# v24 + waves 0-3 only: zero-start sub-head-0 score accumulators via MFMA C=0
# speedup vs baseline: 1.0174x; 1.0079x over previous
.Lc_l2s0:
	s_waitcnt lgkmcnt(5)
	v_mfma_f32_32x32x16_bf16 v[160:175], v[236:239], v[180:183], v[160:175]
	v_add_u32_e32 v7, v212, v231
	s_waitcnt lgkmcnt(4)
	v_mfma_f32_32x32x16_bf16 v[144:159], v[240:243], v[180:183], v[144:159]
	ds_read_b128 v[248:251], v6
	ds_read_b128 v[236:239], v6 offset:8192
	ds_read_b128 v[240:243], v7
	s_waitcnt lgkmcnt(6)
	v_mfma_f32_32x32x16_bf16 v[160:175], v[2:5], v[184:187], v[160:175]
	s_waitcnt lgkmcnt(5)
	v_mfma_f32_32x32x16_bf16 v[144:159], v[8:11], v[184:187], v[144:159]
	s_waitcnt lgkmcnt(4)
	v_mfma_f32_32x32x16_bf16 v[160:175], v[208:211], v[188:191], v[160:175]
	s_waitcnt lgkmcnt(3)
	v_mfma_f32_32x32x16_bf16 v[144:159], v[244:247], v[188:191], v[144:159]
	ds_read_b128 v[244:247], v7 offset:8192
	s_nop 9
	v_exp_f32_e32 v6, v160
	v_exp_f32_e32 v3, v161
	v_exp_f32_e32 v10, v164
	v_exp_f32_e32 v11, v165
	v_exp_f32_e32 v160, v172
	v_exp_f32_e32 v161, v173
	v_exp_f32_e32 v5, v162
	v_exp_f32_e32 v2, v144
	v_exp_f32_e32 v7, v146
	v_exp_f32_e32 v144, v148
	v_exp_f32_e32 v146, v150
	v_exp_f32_e32 v148, v168
	v_exp_f32_e32 v150, v169
	v_exp_f32_e32 v4, v145
	v_exp_f32_e32 v145, v149
	v_exp_f32_e32 v12, v166
	v_exp_f32_e32 v149, v152
	v_exp_f32_e32 v152, v170
	v_exp_f32_e32 v162, v174
	v_exp_f32_e32 v8, v163
	v_exp_f32_e32 v9, v147
	v_exp_f32_e32 v13, v167
	v_exp_f32_e32 v147, v151
	v_exp_f32_e32 v151, v153
	v_exp_f32_e32 v153, v154
	v_exp_f32_e32 v154, v171
	v_exp_f32_e32 v163, v175
	v_exp_f32_e32 v156, v156
	v_exp_f32_e32 v157, v157
	v_add_f32_e32 v164, v6, v3
	v_add_f32_e32 v165, v10, v11
	v_add_f32_e32 v166, v148, v150
	v_add_f32_e32 v167, v160, v161
	v_exp_f32_e32 v158, v158
	v_add_f32_e32 v164, v5, v164
	v_add_f32_e32 v165, v12, v165
	v_add_f32_e32 v166, v152, v166
	v_add_f32_e32 v167, v162, v167
	v_exp_f32_e32 v155, v155
	v_exp_f32_e32 v159, v159
	v_add_f32_e32 v164, v8, v164
	v_add_f32_e32 v165, v13, v165
	v_add_f32_e32 v166, v154, v166
	v_add_f32_e32 v167, v163, v167
	v_add_f32_e32 v164, v2, v164
	v_add_f32_e32 v165, v144, v165
	v_add_f32_e32 v166, v149, v166
	v_add_f32_e32 v167, v156, v167
	v_add_f32_e32 v164, v4, v164
	v_add_f32_e32 v165, v145, v165
	v_add_f32_e32 v166, v151, v166
	v_add_f32_e32 v167, v157, v167
	v_add_f32_e32 v164, v7, v164
	v_add_f32_e32 v165, v146, v165
	v_add_f32_e32 v166, v153, v166
	v_add_f32_e32 v167, v158, v167
	v_add_f32_e32 v164, v9, v164
	v_add_f32_e32 v165, v147, v165
	v_add_f32_e32 v166, v155, v166
	v_add_f32_e32 v167, v159, v167
	v_add_f32_e32 v164, v164, v165
	v_add_f32_e32 v165, v166, v167
	v_add_f32_e32 v213, v164, v165
	v_mov_b32_e32 v218, v213
	v_cvt_pk_bf16_f32 v208, v6, v3
	v_cvt_pk_bf16_f32 v209, v5, v8
	v_cvt_pk_bf16_f32 v210, v10, v11
	v_cvt_pk_bf16_f32 v211, v12, v13
	v_cvt_pk_bf16_f32 v10, v148, v150
	v_cvt_pk_bf16_f32 v11, v152, v154
	v_cvt_pk_bf16_f32 v12, v160, v161
	v_cvt_pk_bf16_f32 v13, v162, v163
	v_cvt_pk_bf16_f32 v6, v2, v4
	v_cvt_pk_bf16_f32 v7, v7, v9
	v_cvt_pk_bf16_f32 v8, v144, v145
	v_cvt_pk_bf16_f32 v9, v146, v147
	v_cvt_pk_bf16_f32 v2, v149, v151
	v_cvt_pk_bf16_f32 v3, v153, v155
	v_cvt_pk_bf16_f32 v4, v156, v157
	v_cvt_pk_bf16_f32 v5, v158, v159
	v_permlane32_swap_b32_e32 v213, v218
	v_permlane32_swap_b32_e32 v208, v210
	v_permlane32_swap_b32_e32 v209, v211
	v_permlane32_swap_b32_e32 v10, v12
	v_permlane32_swap_b32_e32 v11, v13
	v_permlane32_swap_b32_e32 v6, v8
	v_permlane32_swap_b32_e32 v7, v9
	v_permlane32_swap_b32_e32 v2, v4
	v_permlane32_swap_b32_e32 v3, v5
	s_nop 15
	s_nop 15
	v_mov_b32_e32 v160, 0
	s_andn2_b64 vcc, exec, s[44:45]
	v_mov_b32_e32 v161, 0
	v_mov_b32_e32 v162, 0
	v_mov_b32_e32 v163, 0
	v_mov_b32_e32 v164, 0
	v_mov_b32_e32 v165, 0
	v_mov_b32_e32 v166, 0
	v_mov_b32_e32 v167, 0
	v_mov_b32_e32 v168, 0
	v_mov_b32_e32 v169, 0
	v_mov_b32_e32 v170, 0
	v_mov_b32_e32 v171, 0
	v_mov_b32_e32 v172, 0
	v_mov_b32_e32 v173, 0
	v_mov_b32_e32 v174, 0
	v_mov_b32_e32 v175, 0
	v_mov_b32_e32 v144, 0
	v_mov_b32_e32 v145, 0
	v_mov_b32_e32 v146, 0
	v_mov_b32_e32 v147, 0
	v_mov_b32_e32 v148, 0
	v_mov_b32_e32 v149, 0
	v_mov_b32_e32 v150, 0
	v_mov_b32_e32 v151, 0
	v_mov_b32_e32 v152, 0
	v_mov_b32_e32 v153, 0
	v_mov_b32_e32 v154, 0
	v_mov_b32_e32 v155, 0
	v_mov_b32_e32 v156, 0
	v_mov_b32_e32 v157, 0
	v_mov_b32_e32 v158, 0
	v_mov_b32_e32 v159, 0
	s_cbranch_vccnz .LBB0_205
	s_andn2_b64 vcc, exec, s[42:43]
	s_mov_b64 s[42:43], -1
	s_cbranch_vccnz .LBB0_218
	v_add_u32_e32 v146, 0x21780, v219
	v_add_u32_e32 v147, 0x21708, v219
	v_add_u32_e32 v148, 0x21788, v219
	ds_read2_b32 v[144:145], v220 offset1:1
	ds_read2_b32 v[160:161], v146 offset1:1
	ds_read2_b32 v[146:147], v147 offset1:1
	ds_read2_b32 v[162:163], v148 offset1:1
	v_add_u32_e32 v148, 0x21720, v219
	v_add_u32_e32 v150, 0x217a0, v219
	v_add_u32_e32 v151, 0x21728, v219
	v_add_u32_e32 v152, 0x217a8, v219
	ds_read2_b32 v[148:149], v148 offset1:1
	ds_read2_b32 v[164:165], v150 offset1:1
	ds_read2_b32 v[150:151], v151 offset1:1
	ds_read2_b32 v[166:167], v152 offset1:1
	v_add_u32_e32 v152, 0x21740, v219
	v_add_u32_e32 v154, 0x217c0, v219
	v_add_u32_e32 v155, 0x21748, v219
	v_add_u32_e32 v156, 0x217c8, v219
	ds_read2_b32 v[152:153], v152 offset1:1
	ds_read2_b32 v[168:169], v154 offset1:1
	ds_read2_b32 v[154:155], v155 offset1:1
	ds_read2_b32 v[170:171], v156 offset1:1
	v_add_u32_e32 v156, 0x21760, v219
	v_add_u32_e32 v158, 0x217e0, v219
	v_add_u32_e32 v159, 0x21768, v219
	v_add_u32_e32 v174, 0x217e8, v219
	ds_read2_b32 v[156:157], v156 offset1:1
	ds_read2_b32 v[172:173], v158 offset1:1
	ds_read2_b32 v[158:159], v159 offset1:1
	ds_read2_b32 v[174:175], v174 offset1:1
	s_mov_b64 s[42:43], 0
